# baseline (speedup 1.0000x reference)
.Lnorm:
	s_nop 1
	v_mov_b32_e32 v87, v86
	s_nop 1
	v_permlane16_swap_b32_e32 v87, v86
	v_add_f32_e32 v86, v86, v87
	v_mov_b32_e32 v87, v86
	s_nop 1
	v_permlane32_swap_b32_e32 v87, v86
	v_add_f32_e32 v86, v86, v87
	v_mul_f32_e32 v87, 0x4f800000, v86
	v_cmp_gt_f32_e32 vcc, s21, v86
	s_nop 1
	v_cndmask_b32_e32 v86, v86, v87, vcc
	v_sqrt_f32_e32 v87, v86
	s_nop 0
	v_add_u32_e32 v88, -1, v87
	v_fma_f32 v90, -v88, v87, v86
	v_add_u32_e32 v89, 1, v87
	v_cmp_ge_f32_e64 s[12:13], 0, v90
	s_nop 1
	v_cndmask_b32_e64 v88, v87, v88, s[12:13]
	v_fma_f32 v87, -v89, v87, v86
	v_cmp_lt_f32_e64 s[12:13], 0, v87
	s_nop 1
	v_cndmask_b32_e64 v87, v88, v89, s[12:13]
	v_mul_f32_e32 v88, 0x37800000, v87
	v_cndmask_b32_e32 v87, v87, v88, vcc
	v_cmp_class_f32_e32 vcc, v86, v135
	s_nop 1
	v_cndmask_b32_e32 v86, v87, v86, vcc
	v_add_f32_e32 v86, 0x29e12e13, v86
	v_div_scale_f32 v87, s[12:13], v86, v86, 1.0
	v_rcp_f32_e32 v88, v87
	v_lshrrev_b32_e32 v89, s3, v191
	v_and_b32_e32 v89, 1, v89
	s_nop 0
	v_fma_f32 v90, -v87, v88, 1.0
	v_fmac_f32_e32 v88, v90, v88
	v_div_scale_f32 v90, vcc, 1.0, v86, 1.0
	v_mul_f32_e32 v91, v90, v88
	v_fma_f32 v92, -v87, v91, v90
	v_fmac_f32_e32 v91, v92, v88
	v_fma_f32 v87, -v87, v91, v90
	v_div_fmas_f32 v87, v87, v88, v91
	v_div_fixup_f32 v86, v87, v86, 1.0
	v_mul_f32_e32 v86, 0x4166d4ca, v86
	v_cmp_eq_u32_e32 vcc, 1, v89
	s_nop 1
	v_cndmask_b32_e32 v86, 0, v86, vcc
	v_cndmask_b32_e64 v87, v161, 0, vcc
	s_nop 1
	v_mov_b32_dpp v88, v86 row_newbcast:0 row_mask:0x1 bank_mask:0xf
	v_mov_b32_dpp v88, v86 row_newbcast:4 row_mask:0x2 bank_mask:0xf
	v_mov_b32_dpp v88, v86 row_newbcast:8 row_mask:0x4 bank_mask:0xf
	v_mov_b32_dpp v88, v86 row_newbcast:12 row_mask:0x8 bank_mask:0xf
	v_mov_b32_dpp v89, v86 row_newbcast:1 row_mask:0x1 bank_mask:0xf
	v_mov_b32_dpp v89, v86 row_newbcast:5 row_mask:0x2 bank_mask:0xf
	v_mov_b32_dpp v89, v86 row_newbcast:9 row_mask:0x4 bank_mask:0xf
	v_mov_b32_dpp v89, v86 row_newbcast:13 row_mask:0x8 bank_mask:0xf
	v_mov_b32_dpp v90, v87 row_newbcast:0 row_mask:0x1 bank_mask:0xf
	v_mov_b32_dpp v90, v87 row_newbcast:4 row_mask:0x2 bank_mask:0xf
	v_mov_b32_dpp v90, v87 row_newbcast:8 row_mask:0x4 bank_mask:0xf
	v_mov_b32_dpp v90, v87 row_newbcast:12 row_mask:0x8 bank_mask:0xf
	v_mov_b32_dpp v91, v87 row_newbcast:1 row_mask:0x1 bank_mask:0xf
	v_mov_b32_dpp v91, v87 row_newbcast:5 row_mask:0x2 bank_mask:0xf
	v_mov_b32_dpp v91, v87 row_newbcast:9 row_mask:0x4 bank_mask:0xf
	v_mov_b32_dpp v91, v87 row_newbcast:13 row_mask:0x8 bank_mask:0xf
	s_nop 0
	v_mul_f32_e32 v168, v88, v78
	v_mul_f32_e32 v169, v88, v82
	v_pk_mul_f32 v[164:165], v[168:169], s[20:21] op_sel_hi:[1,0]
	v_pk_fma_f32 v[172:173], v[168:169], s[22:23], v[96:97] op_sel_hi:[1,0,0]
	v_pk_fma_f32 v[162:163], v[164:165], v[168:169], v[90:91] op_sel_hi:[1,1,0]
	v_pk_mul_f32 v[164:165], v[172:173], v[172:173] neg_lo:[0,1] neg_hi:[0,1]
	v_exp_f32_e32 v166, v168
	v_exp_f32_e32 v167, v169
	v_exp_f32_e64 v170, -v168
	v_exp_f32_e64 v171, -v169
	v_exp_f32_e32 v162, v162
	v_exp_f32_e32 v164, v164
	v_exp_f32_e32 v165, v165
	v_exp_f32_e32 v163, v163
	v_pk_mul_f32 v[168:169], v[166:167], v[166:167]
	v_pk_mul_f32 v[172:173], v[170:171], v[170:171]
	v_pk_add_f32 v[94:95], v[94:95], v[164:165]
	v_pk_mul_f32 v[164:165], v[166:167], v[162:163]
	v_pk_fma_f32 v[106:107], v[166:167], v[162:163], v[106:107]
	v_pk_mul_f32 v[166:167], v[170:171], v[162:163]
	v_pk_fma_f32 v[108:109], v[170:171], v[162:163], v[108:109]
	v_pk_mul_f32 v[162:163], v[168:169], v[164:165]
	v_pk_fma_f32 v[104:105], v[168:169], v[164:165], v[104:105]
	v_pk_mul_f32 v[164:165], v[172:173], v[166:167]
	v_pk_fma_f32 v[110:111], v[172:173], v[166:167], v[110:111]
	v_pk_mul_f32 v[166:167], v[168:169], v[162:163]
	v_pk_fma_f32 v[102:103], v[168:169], v[162:163], v[102:103]
	v_pk_mul_f32 v[162:163], v[172:173], v[164:165]
	v_pk_fma_f32 v[112:113], v[172:173], v[164:165], v[112:113]
	v_pk_mul_f32 v[164:165], v[168:169], v[166:167]
	v_pk_fma_f32 v[100:101], v[168:169], v[166:167], v[100:101]
	v_pk_mul_f32 v[166:167], v[172:173], v[162:163]
	v_pk_fma_f32 v[114:115], v[172:173], v[162:163], v[114:115]
	v_pk_fma_f32 v[98:99], v[168:169], v[164:165], v[98:99]
	v_pk_fma_f32 v[116:117], v[172:173], v[166:167], v[116:117]
	v_mul_f32_e32 v168, v89, v79
	v_mul_f32_e32 v169, v89, v83
	v_pk_mul_f32 v[164:165], v[168:169], s[20:21] op_sel_hi:[1,0]
	v_pk_fma_f32 v[172:173], v[168:169], s[22:23], v[96:97] op_sel_hi:[1,0,0]
	v_pk_fma_f32 v[162:163], v[164:165], v[168:169], v[90:91] op_sel:[0,0,1] op_sel_hi:[1,1,1]
	v_pk_mul_f32 v[164:165], v[172:173], v[172:173] neg_lo:[0,1] neg_hi:[0,1]
	v_exp_f32_e32 v166, v168
	v_exp_f32_e32 v167, v169
	v_exp_f32_e64 v170, -v168
	v_exp_f32_e64 v171, -v169
	v_exp_f32_e32 v162, v162
	v_exp_f32_e32 v164, v164
	v_exp_f32_e32 v165, v165
	v_exp_f32_e32 v163, v163
	v_pk_mul_f32 v[168:169], v[166:167], v[166:167]
	v_pk_mul_f32 v[172:173], v[170:171], v[170:171]
	v_pk_add_f32 v[94:95], v[94:95], v[164:165]
	v_pk_mul_f32 v[164:165], v[166:167], v[162:163]
	v_pk_fma_f32 v[106:107], v[166:167], v[162:163], v[106:107]
	v_pk_mul_f32 v[166:167], v[170:171], v[162:163]
	v_pk_fma_f32 v[108:109], v[170:171], v[162:163], v[108:109]
	v_pk_mul_f32 v[162:163], v[168:169], v[164:165]
	v_pk_fma_f32 v[104:105], v[168:169], v[164:165], v[104:105]
	v_pk_mul_f32 v[164:165], v[172:173], v[166:167]
	v_pk_fma_f32 v[110:111], v[172:173], v[166:167], v[110:111]
	v_pk_mul_f32 v[166:167], v[168:169], v[162:163]
	v_pk_fma_f32 v[102:103], v[168:169], v[162:163], v[102:103]
	v_pk_mul_f32 v[162:163], v[172:173], v[164:165]
	v_pk_fma_f32 v[112:113], v[172:173], v[164:165], v[112:113]
	v_pk_mul_f32 v[164:165], v[168:169], v[166:167]
	v_pk_fma_f32 v[100:101], v[168:169], v[166:167], v[100:101]
	v_pk_mul_f32 v[166:167], v[172:173], v[162:163]
	v_pk_fma_f32 v[114:115], v[172:173], v[162:163], v[114:115]
	v_pk_fma_f32 v[98:99], v[168:169], v[164:165], v[98:99]
	v_pk_fma_f32 v[116:117], v[172:173], v[166:167], v[116:117]
	s_cmp_eq_u32 s3, 0
	s_cbranch_scc1 .Lret0
	s_cmp_eq_u32 s3, 1
	s_cbranch_scc1 .Lret1
	s_cmp_eq_u32 s3, 2
	s_cbranch_scc1 .Lret2
